# LN2 (layer 0): bf16 x2 stores for the next layer issued write-through (sc0 sc1)
# baseline (speedup 1.0000x reference)
; #define LAS __attribute__((address_space(3)))
; __device__ __forceinline__ void peer_ln2_phase(LAS unsigned char* lds, int wave, int blk, const bf16* __restrict__ X1B, const bf16* __restrict__ YT, const float* __restrict__ g2, const float* __restrict__ b2, ...
;     ...
;     for (int i = 0; i < 8; ++i) {
;         const int tk = wave * 8 + i; const size_t t = (size_t)blk * 64 + tk;
;         float z[16]; float s = 0.f;
; #pragma unroll
;         for (int k = 0; k < 16; ++k) { const float xv = __uint_as_float((unsigned)__builtin_nontemporal_load((const unsigned short*)X1B + t * 1024 + lane + 64 * k) << 16); const unsigned yb = *(const LAS unsigned short*)(lds + (lane + 64 * k) * 136 + tk * 2);
;             z[k] = 1.41421356237309515f * xv + __uint_as_float(yb << 16); s += z[k]; }
; #pragma unroll
;         for (int o = 1; o < 64; o <<= 1) s += __shfl_xor(s, o);
.LBB0_1026:
	v_lshl_add_u64 v[2:3], v[0:1], 0, s[6:7]
	v_add_u32_e32 v47, 0xfffef000, v43
	v_add_u32_e32 v48, 0xffff1200, v43
	v_add_u32_e32 v50, 0xffff5600, v43
	v_add_u32_e32 v51, 0xffff7800, v43
	v_add_u32_e32 v52, 0xffff9a00, v43
	v_add_u32_e32 v53, 0xffffbc00, v43
	v_add_u32_e32 v54, 0xffffde00, v43
	v_add_co_u32_e32 v46, vcc, 0x6000000, v2
	v_add_u32_e32 v49, 0xffff3400, v43
	ds_read_u16 v55, v43
	ds_read_u16 v56, v43 offset:8704
	ds_read_u16 v57, v43 offset:17408
	ds_read_u16 v58, v43 offset:26112
	ds_read_u16 v59, v43 offset:34816
	ds_read_u16 v60, v43 offset:43520
	ds_read_u16 v61, v43 offset:52224
	ds_read_u16 v62, v43 offset:60928
	ds_read_u16 v63, v47
	ds_read_u16 v64, v48
	ds_read_u16 v65, v49
	ds_read_u16 v50, v50
	ds_read_u16 v51, v51
	ds_read_u16 v52, v52
	ds_read_u16 v53, v53
	ds_read_u16 v54, v54
	v_add_co_u32_e64 v48, s[4:5], s10, v2
	v_addc_co_u32_e32 v47, vcc, 0, v3, vcc
	s_nop 0
	v_addc_co_u32_e64 v49, s[4:5], 0, v3, s[4:5]
	global_load_ushort v2, v[46:47], off nt
	global_load_ushort v3, v[46:47], off offset:128 nt
	global_load_ushort v66, v[46:47], off offset:256 nt
	global_load_ushort v67, v[46:47], off offset:384 nt
	global_load_ushort v68, v[46:47], off offset:512 nt
	global_load_ushort v69, v[46:47], off offset:640 nt
	global_load_ushort v70, v[46:47], off offset:768 nt
	global_load_ushort v71, v[46:47], off offset:896 nt
	global_load_ushort v72, v[46:47], off offset:1024 nt
	global_load_ushort v73, v[46:47], off offset:1152 nt
	global_load_ushort v74, v[46:47], off offset:1280 nt
	global_load_ushort v75, v[46:47], off offset:1408 nt
	global_load_ushort v76, v[46:47], off offset:1536 nt
	global_load_ushort v77, v[46:47], off offset:1664 nt
	global_load_ushort v78, v[46:47], off offset:1792 nt
	s_nop 0
	global_load_ushort v46, v[46:47], off offset:1920 nt
	s_waitcnt lgkmcnt(14)
	v_lshlrev_b32_e32 v47, 16, v55
	v_lshlrev_b32_e32 v55, 16, v56
	s_waitcnt lgkmcnt(13)
	v_lshlrev_b32_e32 v56, 16, v57
	s_waitcnt lgkmcnt(12)
	v_lshlrev_b32_e32 v57, 16, v58
	s_waitcnt lgkmcnt(11)
	v_lshlrev_b32_e32 v58, 16, v59
	s_waitcnt lgkmcnt(10)
	v_lshlrev_b32_e32 v59, 16, v60
	s_waitcnt lgkmcnt(9)
	v_lshlrev_b32_e32 v60, 16, v61
	s_waitcnt lgkmcnt(8)
	v_lshlrev_b32_e32 v61, 16, v62
	s_waitcnt lgkmcnt(7)
	v_lshlrev_b32_e32 v62, 16, v63
	s_waitcnt lgkmcnt(6)
	v_lshlrev_b32_e32 v63, 16, v64
	s_waitcnt lgkmcnt(5)
	v_lshlrev_b32_e32 v64, 16, v65
	s_waitcnt lgkmcnt(4)
	v_lshlrev_b32_e32 v50, 16, v50
	s_waitcnt lgkmcnt(3)
	v_lshlrev_b32_e32 v51, 16, v51
	s_waitcnt lgkmcnt(2)
	v_lshlrev_b32_e32 v52, 16, v52
	s_waitcnt lgkmcnt(1)
	v_lshlrev_b32_e32 v53, 16, v53
	s_waitcnt lgkmcnt(0)
	v_lshlrev_b32_e32 v54, 16, v54
	s_add_u32 s6, s6, 0x800
	s_addc_u32 s7, s7, 0
	v_add_u32_e32 v43, 2, v43
	s_cmpk_lg_i32 s6, 0x4000
	s_waitcnt vmcnt(15)
	v_lshlrev_b32_e32 v2, 16, v2
	s_waitcnt vmcnt(14)
	v_lshlrev_b32_e32 v3, 16, v3
	v_fmac_f32_e32 v62, 0x3fb504f3, v2
	s_waitcnt vmcnt(13)
	v_lshlrev_b32_e32 v65, 16, v66
	v_fmac_f32_e32 v63, 0x3fb504f3, v3
	v_add_f32_e32 v2, 0, v62
	s_waitcnt vmcnt(12)
	v_lshlrev_b32_e32 v66, 16, v67
	v_fmac_f32_e32 v64, 0x3fb504f3, v65
	v_add_f32_e32 v2, v2, v63
	s_waitcnt vmcnt(11)
	v_lshlrev_b32_e32 v67, 16, v68
	v_fmac_f32_e32 v50, 0x3fb504f3, v66
	v_add_f32_e32 v2, v2, v64
	s_waitcnt vmcnt(10)
	v_lshlrev_b32_e32 v68, 16, v69
	v_fmac_f32_e32 v51, 0x3fb504f3, v67
	v_add_f32_e32 v2, v2, v50
	s_waitcnt vmcnt(9)
	v_lshlrev_b32_e32 v69, 16, v70
	v_fmac_f32_e32 v52, 0x3fb504f3, v68
	v_add_f32_e32 v2, v2, v51
	s_waitcnt vmcnt(8)
	v_lshlrev_b32_e32 v70, 16, v71
	v_fmac_f32_e32 v53, 0x3fb504f3, v69
	v_add_f32_e32 v2, v2, v52
	s_waitcnt vmcnt(7)
	v_lshlrev_b32_e32 v71, 16, v72
	v_fmac_f32_e32 v54, 0x3fb504f3, v70
	v_add_f32_e32 v2, v2, v53
	s_waitcnt vmcnt(6)
	v_lshlrev_b32_e32 v72, 16, v73
	v_fmac_f32_e32 v47, 0x3fb504f3, v71
	v_add_f32_e32 v2, v2, v54
	s_waitcnt vmcnt(5)
	v_lshlrev_b32_e32 v73, 16, v74
	v_fmac_f32_e32 v55, 0x3fb504f3, v72
	v_add_f32_e32 v2, v2, v47
	s_waitcnt vmcnt(4)
	v_lshlrev_b32_e32 v74, 16, v75
	v_fmac_f32_e32 v56, 0x3fb504f3, v73
	v_add_f32_e32 v2, v2, v55
	s_waitcnt vmcnt(3)
	v_lshlrev_b32_e32 v75, 16, v76
	v_fmac_f32_e32 v57, 0x3fb504f3, v74
	v_add_f32_e32 v2, v2, v56
	s_waitcnt vmcnt(2)
	v_lshlrev_b32_e32 v76, 16, v77
	v_fmac_f32_e32 v58, 0x3fb504f3, v75
	v_add_f32_e32 v2, v2, v57
	s_waitcnt vmcnt(1)
	v_lshlrev_b32_e32 v77, 16, v78
	v_fmac_f32_e32 v59, 0x3fb504f3, v76
	v_add_f32_e32 v2, v2, v58
	s_waitcnt vmcnt(0)
; #define GAS __attribute__((address_space(1)))
; __device__ __forceinline__ unsigned f2bf(float f) { unsigned u = __builtin_bit_cast(unsigned, f); return (u + 0x7fffu + ((u >> 16) & 1u)) >> 16; }
; __device__ __forceinline__ void peer_ln2_phase(LAS unsigned char* lds, int wave, int blk, const bf16* __restrict__ X1B, const bf16* __restrict__ YT, const float* __restrict__ g2, const float* __restrict__ b2, ...
;     ...
;             z[k] = 1.41421356237309515f * xv + __uint_as_float(yb << 16); s += z[k]; }
; #pragma unroll
;         for (int o = 1; o < 64; o <<= 1) s += __shfl_xor(s, o);
;         const float mean = s * (1.0f / 1024.0f); float sq = 0.f;
; #pragma unroll
;         for (int k = 0; k < 16; ++k) { z[k] -= mean; sq += z[k] * z[k]; }
; #pragma unroll
;         for (int o = 1; o < 64; o <<= 1) sq += __shfl_xor(sq, o);
;         const float rstd = 1.0f / sqrtf(sq * (1.0f / 1024.0f) + 1e-5f);
; #pragma unroll
;         for (int k = 0; k < 16; ++k) { z[k] = z[k] * rstd * gv[k] + bv[k]; if (outf) __builtin_nontemporal_store(z[k], outf + t * 1024 + lane + 64 * k); }
;         if (outb) {
; #pragma unroll
;             for (int k = 0; k < 16; ++k) ((GAS unsigned short*)outb)[t * 1024 + lane + 64 * k] = (unsigned short)f2bf(z[k]); }
	v_lshlrev_b32_e32 v46, 16, v46
	v_fmac_f32_e32 v60, 0x3fb504f3, v77
	v_add_f32_e32 v2, v2, v59
	v_fmac_f32_e32 v61, 0x3fb504f3, v46
	v_add_f32_e32 v2, v2, v60
	v_add_f32_e32 v2, v2, v61
	s_nop 1
	v_add_f32_dpp v2, v2, v2 row_shr:1 row_mask:0xf bank_mask:0xf
	s_nop 1
	v_add_f32_dpp v2, v2, v2 row_shr:2 row_mask:0xf bank_mask:0xf
	s_nop 1
	v_add_f32_dpp v2, v2, v2 row_shr:4 row_mask:0xf bank_mask:0xf
	s_nop 1
	v_add_f32_dpp v2, v2, v2 row_shr:8 row_mask:0xf bank_mask:0xf
	s_nop 1
	v_add_f32_dpp v2, v2, v2 row_bcast:15 row_mask:0xa bank_mask:0xf
	s_nop 1
	v_add_f32_dpp v2, v2, v2 row_bcast:31 row_mask:0xc bank_mask:0xf
	s_nop 1
	v_readlane_b32 s98, v2, 63
	s_nop 1
	v_mov_b32_e32 v2, s98
	v_fmac_f32_e32 v63, 0xba800000, v2
	v_fmac_f32_e32 v62, 0xba800000, v2
	v_fmac_f32_e32 v64, 0xba800000, v2
	v_fmac_f32_e32 v50, 0xba800000, v2
	v_fmac_f32_e32 v51, 0xba800000, v2
	v_fmac_f32_e32 v52, 0xba800000, v2
	v_fmac_f32_e32 v53, 0xba800000, v2
	v_fmac_f32_e32 v54, 0xba800000, v2
	v_fmac_f32_e32 v47, 0xba800000, v2
	v_fmac_f32_e32 v55, 0xba800000, v2
	v_fmac_f32_e32 v56, 0xba800000, v2
	v_fmac_f32_e32 v57, 0xba800000, v2
	v_fmac_f32_e32 v58, 0xba800000, v2
	v_fmac_f32_e32 v59, 0xba800000, v2
	v_fmac_f32_e32 v60, 0xba800000, v2
	v_fmac_f32_e32 v61, 0xba800000, v2
	v_mul_f32_e32 v2, v63, v63
	v_fmac_f32_e32 v2, v62, v62
	v_fmac_f32_e32 v2, v64, v64
	v_fmac_f32_e32 v2, v50, v50
	v_fmac_f32_e32 v2, v51, v51
	v_fmac_f32_e32 v2, v52, v52
	v_fmac_f32_e32 v2, v53, v53
	v_fmac_f32_e32 v2, v54, v54
	v_fmac_f32_e32 v2, v47, v47
	v_fmac_f32_e32 v2, v55, v55
	v_fmac_f32_e32 v2, v56, v56
	v_fmac_f32_e32 v2, v57, v57
	v_fmac_f32_e32 v2, v58, v58
	v_fmac_f32_e32 v2, v59, v59
	v_fmac_f32_e32 v2, v60, v60
	v_fmac_f32_e32 v2, v61, v61
	s_nop 1
	v_add_f32_dpp v2, v2, v2 row_shr:1 row_mask:0xf bank_mask:0xf
	s_nop 1
	v_add_f32_dpp v2, v2, v2 row_shr:2 row_mask:0xf bank_mask:0xf
	s_nop 1
	v_add_f32_dpp v2, v2, v2 row_shr:4 row_mask:0xf bank_mask:0xf
	s_nop 1
	v_add_f32_dpp v2, v2, v2 row_shr:8 row_mask:0xf bank_mask:0xf
	s_nop 1
	v_add_f32_dpp v2, v2, v2 row_bcast:15 row_mask:0xa bank_mask:0xf
	s_nop 1
	v_add_f32_dpp v2, v2, v2 row_bcast:31 row_mask:0xc bank_mask:0xf
	s_nop 1
	v_readlane_b32 s98, v2, 63
	s_nop 1
	v_mov_b32_e32 v2, s98
	v_fmamk_f32 v2, v2, 0x3a800000, v44
	v_mul_f32_e32 v3, 0x4f800000, v2
	v_cmp_gt_f32_e32 vcc, s8, v2
	s_nop 1
	v_cndmask_b32_e32 v2, v2, v3, vcc
	v_sqrt_f32_e32 v3, v2
	s_nop 0
	v_add_u32_e32 v46, -1, v3
	v_add_u32_e32 v65, 1, v3
	v_fma_f32 v66, -v46, v3, v2
	v_fma_f32 v67, -v65, v3, v2
	v_cmp_ge_f32_e64 s[4:5], 0, v66
	s_nop 1
	v_cndmask_b32_e64 v3, v3, v46, s[4:5]
	v_cmp_lt_f32_e64 s[4:5], 0, v67
	s_nop 1
	v_cndmask_b32_e64 v3, v3, v65, s[4:5]
	v_mul_f32_e32 v46, 0x37800000, v3
	v_cndmask_b32_e32 v3, v3, v46, vcc
	v_cmp_class_f32_e32 vcc, v2, v45
	s_nop 1
	v_cndmask_b32_e32 v2, v3, v2, vcc
	v_div_scale_f32 v3, s[4:5], v2, v2, 1.0
	v_rcp_f32_e32 v65, v3
	v_div_scale_f32 v46, vcc, 1.0, v2, 1.0
	v_fma_f32 v66, -v3, v65, 1.0
	v_fmac_f32_e32 v65, v66, v65
	v_mul_f32_e32 v66, v46, v65
	v_fma_f32 v67, -v3, v66, v46
	v_fmac_f32_e32 v66, v67, v65
	v_fma_f32 v3, -v3, v66, v46
	v_div_fmas_f32 v3, v3, v65, v66
	v_div_fixup_f32 v2, v3, v2, 1.0
	v_mul_f32_e32 v3, v62, v2
	v_mul_f32_e32 v46, v63, v2
	v_mul_f32_e32 v62, v64, v2
	v_mul_f32_e32 v50, v50, v2
	v_mul_f32_e32 v51, v51, v2
	v_mul_f32_e32 v52, v52, v2
	v_mul_f32_e32 v53, v53, v2
	v_mul_f32_e32 v54, v54, v2
	v_mul_f32_e32 v47, v47, v2
	v_mul_f32_e32 v55, v55, v2
	v_mul_f32_e32 v56, v56, v2
	v_mul_f32_e32 v57, v57, v2
	v_mul_f32_e32 v58, v58, v2
	v_mul_f32_e32 v59, v59, v2
	v_mul_f32_e32 v60, v60, v2
	v_mul_f32_e32 v2, v61, v2
	v_fma_f32 v3, v4, v3, v13
	v_fma_f32 v46, v5, v46, v14
	v_fma_f32 v61, v6, v62, v15
	v_fma_f32 v50, v7, v50, v16
	v_fma_f32 v51, v9, v51, v17
	v_fma_f32 v52, v10, v52, v18
	v_fma_f32 v53, v11, v53, v19
	v_fma_f32 v54, v12, v54, v20
	v_fma_f32 v47, v21, v47, v29
	v_fma_f32 v55, v22, v55, v30
	v_fma_f32 v56, v23, v56, v31
	v_fma_f32 v57, v24, v57, v32
	v_fma_f32 v58, v25, v58, v33
	v_fma_f32 v59, v26, v59, v34
	v_fma_f32 v60, v27, v60, v35
	v_fma_f32 v2, v28, v2, v36
	v_bfe_u32 v62, v3, 16, 1
	v_bfe_u32 v63, v46, 16, 1
	v_bfe_u32 v64, v61, 16, 1
	v_bfe_u32 v65, v50, 16, 1
	v_bfe_u32 v66, v51, 16, 1
	v_bfe_u32 v67, v52, 16, 1
	v_bfe_u32 v68, v53, 16, 1
	v_bfe_u32 v69, v54, 16, 1
	v_bfe_u32 v70, v47, 16, 1
	v_bfe_u32 v71, v55, 16, 1
	v_bfe_u32 v72, v56, 16, 1
	v_bfe_u32 v73, v57, 16, 1
	v_bfe_u32 v74, v58, 16, 1
	v_bfe_u32 v75, v59, 16, 1
	v_bfe_u32 v76, v60, 16, 1
	v_bfe_u32 v77, v2, 16, 1
	v_add3_u32 v3, v3, v62, s9
	v_add3_u32 v46, v46, v63, s9
	v_add3_u32 v61, v61, v64, s9
	v_add3_u32 v50, v50, v65, s9
	v_add3_u32 v51, v51, v66, s9
	v_add3_u32 v52, v52, v67, s9
	v_add3_u32 v53, v53, v68, s9
	v_add3_u32 v54, v54, v69, s9
	v_add3_u32 v47, v47, v70, s9
	v_add3_u32 v55, v55, v71, s9
	v_add3_u32 v56, v56, v72, s9
	v_add3_u32 v57, v57, v73, s9
	v_add3_u32 v58, v58, v74, s9
	v_add3_u32 v59, v59, v75, s9
	v_add3_u32 v60, v60, v76, s9
	v_add3_u32 v2, v2, v77, s9
	global_store_short_d16_hi v[48:49], v3, off sc0 sc1
	global_store_short_d16_hi v[48:49], v46, off offset:128 sc0 sc1
	global_store_short_d16_hi v[48:49], v61, off offset:256 sc0 sc1
	global_store_short_d16_hi v[48:49], v50, off offset:384 sc0 sc1
	global_store_short_d16_hi v[48:49], v51, off offset:512 sc0 sc1
	global_store_short_d16_hi v[48:49], v52, off offset:640 sc0 sc1
	global_store_short_d16_hi v[48:49], v53, off offset:768 sc0 sc1
	global_store_short_d16_hi v[48:49], v54, off offset:896 sc0 sc1
	global_store_short_d16_hi v[48:49], v47, off offset:1024 sc0 sc1
	global_store_short_d16_hi v[48:49], v55, off offset:1152 sc0 sc1
	global_store_short_d16_hi v[48:49], v56, off offset:1280 sc0 sc1
	global_store_short_d16_hi v[48:49], v57, off offset:1408 sc0 sc1
	global_store_short_d16_hi v[48:49], v58, off offset:1536 sc0 sc1
	global_store_short_d16_hi v[48:49], v59, off offset:1664 sc0 sc1
	global_store_short_d16_hi v[48:49], v60, off offset:1792 sc0 sc1
	global_store_short_d16_hi v[48:49], v2, off offset:1920 sc0 sc1
	s_cbranch_scc1 .LBB0_1026
; __device__ __forceinline__ int mk_lane() { int l_ = (int)__builtin_amdgcn_mbcnt_hi(~0u, __builtin_amdgcn_mbcnt_lo(~0u, 0u)); asm volatile("" : "+v"(l_)); return l_; }
; #define BOTH(k) (IN(k) && IN((k) + 1))
; __device__ __forceinline__ void xcd_barrier(const XcdBarrier& b, int wave_id, int pair = -1) {
;     asm volatile("s_waitcnt vmcnt(0)" ::: "memory");
;     __syncthreads();
;     if (wave_id == 0 && mk_lane() == 0) {
;         unsigned* bar = b.bar;
;         __builtin_amdgcn_s_waitcnt(0);
;         unsigned nloc = b.st[0], nx = b.st[1];
;         if (nloc == 0u) { xcd_barrier_complete(bar, b.x, nloc, nx); b.st[0] = nloc; b.st[1] = nx; }
; template <int K> __device__ __forceinline__ void run_phase(Frame& F, const XcdBarrier& bar, int lo, int hi, unsigned char* lds) {
;     ...
;         if (BOTH(k)) {
;             constexpr bool LOCAL_SEAM = MK_LOCALBAR && (sub == 2 || (sub == 6 && l == 0));
;             bool local = false;
;             if (LOCAL_SEAM) local = __hip_atomic_load((unsigned*)(F.ctl + CW_LBAR + 24 * 64), __ATOMIC_RELAXED, __HIP_MEMORY_SCOPE_AGENT) == 0u;
;             constexpr bool PAIR_SEAM = MK_LOCALBAR && (sub == 0 || sub == 1);
;             bool pairok = false;
;             if (PAIR_SEAM) pairok = __hip_atomic_load((unsigned*)(F.ctl + CW_LBAR + 24 * 64), __ATOMIC_RELAXED, __HIP_MEMORY_SCOPE_AGENT) == 0u;
;             if (local) xcd_local_barrier((unsigned*)(F.ctl + CW_LBAR + ((sub == 2 ? l : 2) * 8 + (bx & 7)) * 64), (unsigned)(G >> 3), (unsigned*)(F.ctl + CW_BAR) + XB_TMO, F.wave);
;             else xcd_barrier(bar, F.wave, pairok ? ((bx & 7) >> 1) : -1);
	s_cmp_lt_u32 s41, 9
	s_barrier
	s_cbranch_scc1 .LBB0_1106
	v_mov_b32_e32 v0, 0x31000
	global_load_dword v0, v0, s[30:31] offset:2048 sc1
	s_waitcnt vmcnt(0)
	v_cmp_ne_u32_e32 vcc, 0, v0
	s_cbranch_vccz .LBB0_1041
	s_waitcnt vmcnt(0)
	s_andn2_b64 vcc, exec, s[38:39]
	s_barrier
	s_cbranch_vccnz .LBB0_1084
	v_mov_b32_e32 v0, v8
	s_nop 0
	v_cmp_eq_u32_e32 vcc, 0, v0
	s_and_saveexec_b64 s[4:5], vcc
	s_cbranch_execz .LBB0_1083
	s_add_i32 s6, 0, 0x27f60
	v_mov_b32_e32 v0, s6
	s_waitcnt vmcnt(0) expcnt(0) lgkmcnt(0)
	ds_read_b32 v2, v0
	s_add_i32 s6, 0, 0x27f64
	v_mov_b32_e32 v0, s6
	ds_read_b32 v0, v0
	s_waitcnt lgkmcnt(1)
	v_cmp_ne_u32_e32 vcc, 0, v2
	s_cbranch_vccnz .LBB0_1047
	v_readlane_b32 s6, v248, 0
	v_readlane_b32 s7, v248, 1
	s_load_dwordx2 s[10:11], s[6:7], 0x4
	s_add_u32 s6, s30, 0x4200
	s_addc_u32 s7, s31, 0
	s_add_u32 s8, s30, 0x4400
	s_addc_u32 s9, s31, 0
	s_waitcnt lgkmcnt(0)
	s_mul_i32 s59, s10, s60
	s_add_u32 s10, s30, 0x4500
	s_mul_i32 s59, s59, s11
	s_addc_u32 s11, s31, 0
	s_add_u32 s12, s30, 0x4600
	s_addc_u32 s13, s31, 0
	s_add_u32 s14, s30, 0x4700
	s_addc_u32 s15, s31, 0
	s_add_u32 s16, s30, 0x4800
	s_addc_u32 s17, s31, 0
	s_add_u32 s18, s30, 0x4900
	s_addc_u32 s19, s31, 0
	s_add_u32 s20, s30, 0x4a00
	s_addc_u32 s21, s31, 0
	s_add_u32 s22, s30, 0x4b00
	s_addc_u32 s23, s31, 0
	s_add_u32 s24, s30, 0x4c00
	s_addc_u32 s25, s31, 0
	s_add_u32 s26, s30, 0x4d00
	s_addc_u32 s27, s31, 0
	s_add_u32 s28, s30, 0x4e00
	s_addc_u32 s29, s31, 0
	s_add_u32 s42, s30, 0x4f00
	s_addc_u32 s43, s31, 0
	s_add_u32 s44, s30, 0x5000
	s_addc_u32 s45, s31, 0
	s_add_u32 s46, s30, 0x5100
	s_addc_u32 s47, s31, 0
	s_add_u32 s48, s30, 0x5200
	s_addc_u32 s49, s31, 0
	s_add_u32 s50, s30, 0x5300
	s_addc_u32 s51, s31, 0
	s_mov_b32 s62, 1
	v_mov_b32_e32 v17, 0
	s_branch .LBB0_1034
